# grid barrier: XCD leader publishes the per-XCD generation word before its own L1 acquire (invalidate moved after the publish), 18 barrier sites
# baseline (speedup 1.0000x reference)
; __device__ __forceinline__ unsigned xb_ld(unsigned* p)              { return __hip_atomic_load(p, __ATOMIC_RELAXED, __HIP_MEMORY_SCOPE_AGENT); }
; __device__ __forceinline__ unsigned xb_add(unsigned* p, unsigned v) { return __hip_atomic_fetch_add(p, v, __ATOMIC_RELAXED, __HIP_MEMORY_SCOPE_AGENT); }
; #define XB_SPIN(cond, bar) do { unsigned _sp = 0; while (cond) { __builtin_amdgcn_s_sleep(1); \
;     if ((++_sp & 255u) == 0u) { if (xb_ld(&(bar)[XB_TMO])) break; if (_sp > XB_SPIN_CAP) { atomicAdd(&(bar)[XB_TMO], 1u); break; } } } } while (0)
; __device__ __forceinline__ void xcd_barrier(const XcdBarrier& b) {
;     ...
;         const unsigned old = xb_add(&bar[XB_XSUB(b.x)], 1u);
;         const unsigned gen = old / nloc;
;         if (old + 1u == (gen + 1u) * nloc) {
;             __builtin_amdgcn_fence(__ATOMIC_RELEASE, "agent");
;             asm volatile("s_waitcnt vmcnt(0)" ::: "memory");
;             const unsigned og = xb_add(&bar[XB_TOP], 1u);
;             const unsigned tg = og / nx;
;             if (og + 1u == (tg + 1u) * nx) xb_add(&bar[XB_TOPGEN], 1u);
;             else XB_SPIN(xb_ld(&bar[XB_TOPGEN]) == tg, bar);
;             __builtin_amdgcn_fence(__ATOMIC_ACQUIRE, "agent");
;             xb_add(&bar[XB_XGEN(b.x)], 1u);
;             asm volatile("s_waitcnt vmcnt(0)" ::: "memory");
;         } else {
;             XB_SPIN(xb_ld(&bar[XB_XGEN(b.x)]) == gen, bar);
;             __builtin_amdgcn_fence(__ATOMIC_ACQUIRE, "agent");
;             asm volatile("s_waitcnt vmcnt(0)" ::: "memory");
.LBB0_190:
	s_or_b64 exec, exec, s[10:11]
	s_mov_b64 s[10:11], exec
	v_mbcnt_lo_u32_b32 v0, s10, 0
	v_mbcnt_hi_u32_b32 v0, s11, v0
	v_cmp_eq_u32_e32 vcc, 0, v0
	s_and_saveexec_b64 s[12:13], vcc
	s_cbranch_execz .LBB0_192
	s_bcnt1_i32_b64 s3, s[10:11]
	v_mov_b32_e32 v0, 0x2000
	v_mov_b32_e32 v1, s3
	global_atomic_add v0, v1, s[8:9] offset:1024
.LBB0_192:
	s_or_b64 exec, exec, s[12:13]
	s_waitcnt vmcnt(0)
	buffer_inv sc1
	s_waitcnt vmcnt(0)
.LBB0_193:
	s_or_b64 exec, exec, s[6:7]
	s_waitcnt lgkmcnt(0)
	s_barrier

; __device__ __forceinline__ unsigned xb_ld(unsigned* p)              { return __hip_atomic_load(p, __ATOMIC_RELAXED, __HIP_MEMORY_SCOPE_AGENT); }
; __device__ __forceinline__ unsigned xb_add(unsigned* p, unsigned v) { return __hip_atomic_fetch_add(p, v, __ATOMIC_RELAXED, __HIP_MEMORY_SCOPE_AGENT); }
; #define XB_SPIN(cond, bar) do { unsigned _sp = 0; while (cond) { __builtin_amdgcn_s_sleep(1); \
;     if ((++_sp & 255u) == 0u) { if (xb_ld(&(bar)[XB_TMO])) break; if (_sp > XB_SPIN_CAP) { atomicAdd(&(bar)[XB_TMO], 1u); break; } } } } while (0)
; __device__ __forceinline__ void xcd_barrier(const XcdBarrier& b) {
;     ...
;             __builtin_amdgcn_fence(__ATOMIC_ACQUIRE, "agent");
;             xb_add(&bar[XB_XGEN(b.x)], 1u);
;             asm volatile("s_waitcnt vmcnt(0)" ::: "memory");
;         } else {
;             XB_SPIN(xb_ld(&bar[XB_XGEN(b.x)]) == gen, bar);
;             __builtin_amdgcn_fence(__ATOMIC_ACQUIRE, "agent");
;             asm volatile("s_waitcnt vmcnt(0)" ::: "memory");
.LBB0_357:
	s_or_b64 exec, exec, s[12:13]
	s_waitcnt vmcnt(0)
	buffer_inv sc1
	s_waitcnt vmcnt(0)
.LBB0_358:
	s_or_b64 exec, exec, s[6:7]
	s_waitcnt lgkmcnt(0)
	s_barrier

; __device__ __forceinline__ unsigned xb_ld(unsigned* p)              { return __hip_atomic_load(p, __ATOMIC_RELAXED, __HIP_MEMORY_SCOPE_AGENT); }
; __device__ __forceinline__ unsigned xb_add(unsigned* p, unsigned v) { return __hip_atomic_fetch_add(p, v, __ATOMIC_RELAXED, __HIP_MEMORY_SCOPE_AGENT); }
; #define XB_SPIN(cond, bar) do { unsigned _sp = 0; while (cond) { __builtin_amdgcn_s_sleep(1); \
;     if ((++_sp & 255u) == 0u) { if (xb_ld(&(bar)[XB_TMO])) break; if (_sp > XB_SPIN_CAP) { atomicAdd(&(bar)[XB_TMO], 1u); break; } } } } while (0)
; __device__ __forceinline__ void xcd_barrier(const XcdBarrier& b) {
;     ...
;             __builtin_amdgcn_fence(__ATOMIC_ACQUIRE, "agent");
;             xb_add(&bar[XB_XGEN(b.x)], 1u);
;             asm volatile("s_waitcnt vmcnt(0)" ::: "memory");
;         } else {
;             XB_SPIN(xb_ld(&bar[XB_XGEN(b.x)]) == gen, bar);
;             __builtin_amdgcn_fence(__ATOMIC_ACQUIRE, "agent");
;             asm volatile("s_waitcnt vmcnt(0)" ::: "memory");
.LBB0_468:
	s_or_b64 exec, exec, s[12:13]
	s_waitcnt vmcnt(0)
	buffer_inv sc1
	s_waitcnt vmcnt(0)
.LBB0_469:
	s_or_b64 exec, exec, s[6:7]
	s_waitcnt lgkmcnt(0)
	s_barrier

; __device__ __forceinline__ unsigned xb_ld(unsigned* p)              { return __hip_atomic_load(p, __ATOMIC_RELAXED, __HIP_MEMORY_SCOPE_AGENT); }
; __device__ __forceinline__ unsigned xb_add(unsigned* p, unsigned v) { return __hip_atomic_fetch_add(p, v, __ATOMIC_RELAXED, __HIP_MEMORY_SCOPE_AGENT); }
; #define XB_SPIN(cond, bar) do { unsigned _sp = 0; while (cond) { __builtin_amdgcn_s_sleep(1); \
;     if ((++_sp & 255u) == 0u) { if (xb_ld(&(bar)[XB_TMO])) break; if (_sp > XB_SPIN_CAP) { atomicAdd(&(bar)[XB_TMO], 1u); break; } } } } while (0)
; __device__ __forceinline__ void xcd_barrier(const XcdBarrier& b) {
;     ...
;             __builtin_amdgcn_fence(__ATOMIC_ACQUIRE, "agent");
;             xb_add(&bar[XB_XGEN(b.x)], 1u);
;             asm volatile("s_waitcnt vmcnt(0)" ::: "memory");
;         } else {
;             XB_SPIN(xb_ld(&bar[XB_XGEN(b.x)]) == gen, bar);
;             __builtin_amdgcn_fence(__ATOMIC_ACQUIRE, "agent");
;             asm volatile("s_waitcnt vmcnt(0)" ::: "memory");
.LBB0_549:
	s_or_b64 exec, exec, s[12:13]
	s_waitcnt vmcnt(0)
	buffer_inv sc1
	s_waitcnt vmcnt(0)
.LBB0_550:
	s_or_b64 exec, exec, s[6:7]
	s_waitcnt lgkmcnt(0)
	s_barrier

; __device__ __forceinline__ unsigned xb_ld(unsigned* p)              { return __hip_atomic_load(p, __ATOMIC_RELAXED, __HIP_MEMORY_SCOPE_AGENT); }
; __device__ __forceinline__ unsigned xb_add(unsigned* p, unsigned v) { return __hip_atomic_fetch_add(p, v, __ATOMIC_RELAXED, __HIP_MEMORY_SCOPE_AGENT); }
; #define XB_SPIN(cond, bar) do { unsigned _sp = 0; while (cond) { __builtin_amdgcn_s_sleep(1); \
;     if ((++_sp & 255u) == 0u) { if (xb_ld(&(bar)[XB_TMO])) break; if (_sp > XB_SPIN_CAP) { atomicAdd(&(bar)[XB_TMO], 1u); break; } } } } while (0)
; __device__ __forceinline__ void xcd_barrier(const XcdBarrier& b) {
;     ...
;             __builtin_amdgcn_fence(__ATOMIC_ACQUIRE, "agent");
;             xb_add(&bar[XB_XGEN(b.x)], 1u);
;             asm volatile("s_waitcnt vmcnt(0)" ::: "memory");
;         } else {
;             XB_SPIN(xb_ld(&bar[XB_XGEN(b.x)]) == gen, bar);
;             __builtin_amdgcn_fence(__ATOMIC_ACQUIRE, "agent");
;             asm volatile("s_waitcnt vmcnt(0)" ::: "memory");
.LBB0_628:
	s_or_b64 exec, exec, s[12:13]
	s_waitcnt vmcnt(0)
	buffer_inv sc1
	s_waitcnt vmcnt(0)
.LBB0_629:
	s_or_b64 exec, exec, s[6:7]
	s_waitcnt lgkmcnt(0)
	s_barrier

; __device__ __forceinline__ unsigned xb_ld(unsigned* p)              { return __hip_atomic_load(p, __ATOMIC_RELAXED, __HIP_MEMORY_SCOPE_AGENT); }
; __device__ __forceinline__ unsigned xb_add(unsigned* p, unsigned v) { return __hip_atomic_fetch_add(p, v, __ATOMIC_RELAXED, __HIP_MEMORY_SCOPE_AGENT); }
; #define XB_SPIN(cond, bar) do { unsigned _sp = 0; while (cond) { __builtin_amdgcn_s_sleep(1); \
;     if ((++_sp & 255u) == 0u) { if (xb_ld(&(bar)[XB_TMO])) break; if (_sp > XB_SPIN_CAP) { atomicAdd(&(bar)[XB_TMO], 1u); break; } } } } while (0)
; __device__ __forceinline__ void xcd_barrier(const XcdBarrier& b) {
;     ...
;             __builtin_amdgcn_fence(__ATOMIC_ACQUIRE, "agent");
;             xb_add(&bar[XB_XGEN(b.x)], 1u);
;             asm volatile("s_waitcnt vmcnt(0)" ::: "memory");
;         } else {
;             XB_SPIN(xb_ld(&bar[XB_XGEN(b.x)]) == gen, bar);
;             __builtin_amdgcn_fence(__ATOMIC_ACQUIRE, "agent");
;             asm volatile("s_waitcnt vmcnt(0)" ::: "memory");
.LBB0_686:
	s_or_b64 exec, exec, s[8:9]
	s_mov_b64 s[8:9], exec
	v_mbcnt_lo_u32_b32 v0, s8, 0
	v_mbcnt_hi_u32_b32 v0, s9, v0
	v_cmp_eq_u32_e32 vcc, 0, v0
	s_and_saveexec_b64 s[10:11], vcc
	s_cbranch_execz .LBB0_688
	s_bcnt1_i32_b64 s3, s[8:9]
	v_mov_b32_e32 v0, 0x2000
	v_mov_b32_e32 v1, s3
	global_atomic_add v0, v1, s[6:7] offset:1024
.LBB0_688:
	s_or_b64 exec, exec, s[10:11]
	s_waitcnt vmcnt(0)
	buffer_inv sc1
	s_waitcnt vmcnt(0)
.LBB0_689:
	s_or_b64 exec, exec, s[4:5]
	s_waitcnt lgkmcnt(0)
	s_barrier

; __device__ __forceinline__ unsigned xb_ld(unsigned* p)              { return __hip_atomic_load(p, __ATOMIC_RELAXED, __HIP_MEMORY_SCOPE_AGENT); }
; __device__ __forceinline__ unsigned xb_add(unsigned* p, unsigned v) { return __hip_atomic_fetch_add(p, v, __ATOMIC_RELAXED, __HIP_MEMORY_SCOPE_AGENT); }
; #define XB_SPIN(cond, bar) do { unsigned _sp = 0; while (cond) { __builtin_amdgcn_s_sleep(1); \
;     if ((++_sp & 255u) == 0u) { if (xb_ld(&(bar)[XB_TMO])) break; if (_sp > XB_SPIN_CAP) { atomicAdd(&(bar)[XB_TMO], 1u); break; } } } } while (0)
; __device__ __forceinline__ void xcd_barrier(const XcdBarrier& b) {
;     ...
;             __builtin_amdgcn_fence(__ATOMIC_ACQUIRE, "agent");
;             xb_add(&bar[XB_XGEN(b.x)], 1u);
;             asm volatile("s_waitcnt vmcnt(0)" ::: "memory");
;         } else {
;             XB_SPIN(xb_ld(&bar[XB_XGEN(b.x)]) == gen, bar);
;             __builtin_amdgcn_fence(__ATOMIC_ACQUIRE, "agent");
;             asm volatile("s_waitcnt vmcnt(0)" ::: "memory");
.LBB0_783:
	s_or_b64 exec, exec, s[12:13]
	s_waitcnt vmcnt(0)
	buffer_inv sc1
	s_waitcnt vmcnt(0)
.LBB0_784:
	s_or_b64 exec, exec, s[6:7]
	s_waitcnt lgkmcnt(0)
	s_barrier

; __device__ __forceinline__ unsigned xb_ld(unsigned* p)              { return __hip_atomic_load(p, __ATOMIC_RELAXED, __HIP_MEMORY_SCOPE_AGENT); }
; __device__ __forceinline__ unsigned xb_add(unsigned* p, unsigned v) { return __hip_atomic_fetch_add(p, v, __ATOMIC_RELAXED, __HIP_MEMORY_SCOPE_AGENT); }
; #define XB_SPIN(cond, bar) do { unsigned _sp = 0; while (cond) { __builtin_amdgcn_s_sleep(1); \
;     if ((++_sp & 255u) == 0u) { if (xb_ld(&(bar)[XB_TMO])) break; if (_sp > XB_SPIN_CAP) { atomicAdd(&(bar)[XB_TMO], 1u); break; } } } } while (0)
; __device__ __forceinline__ void xcd_barrier(const XcdBarrier& b) {
;     ...
;             __builtin_amdgcn_fence(__ATOMIC_ACQUIRE, "agent");
;             xb_add(&bar[XB_XGEN(b.x)], 1u);
;             asm volatile("s_waitcnt vmcnt(0)" ::: "memory");
;         } else {
;             XB_SPIN(xb_ld(&bar[XB_XGEN(b.x)]) == gen, bar);
;             __builtin_amdgcn_fence(__ATOMIC_ACQUIRE, "agent");
;             asm volatile("s_waitcnt vmcnt(0)" ::: "memory");
.LBB0_868:
	s_or_b64 exec, exec, s[12:13]
	s_waitcnt vmcnt(0)
	buffer_inv sc1
	s_waitcnt vmcnt(0)
.LBB0_869:
	s_or_b64 exec, exec, s[6:7]
	s_waitcnt lgkmcnt(0)
	s_barrier

; __device__ __forceinline__ unsigned xb_ld(unsigned* p)              { return __hip_atomic_load(p, __ATOMIC_RELAXED, __HIP_MEMORY_SCOPE_AGENT); }
; __device__ __forceinline__ unsigned xb_add(unsigned* p, unsigned v) { return __hip_atomic_fetch_add(p, v, __ATOMIC_RELAXED, __HIP_MEMORY_SCOPE_AGENT); }
; #define XB_SPIN(cond, bar) do { unsigned _sp = 0; while (cond) { __builtin_amdgcn_s_sleep(1); \
;     if ((++_sp & 255u) == 0u) { if (xb_ld(&(bar)[XB_TMO])) break; if (_sp > XB_SPIN_CAP) { atomicAdd(&(bar)[XB_TMO], 1u); break; } } } } while (0)
; __device__ __forceinline__ void xcd_barrier(const XcdBarrier& b) {
;     ...
;             __builtin_amdgcn_fence(__ATOMIC_ACQUIRE, "agent");
;             xb_add(&bar[XB_XGEN(b.x)], 1u);
;             asm volatile("s_waitcnt vmcnt(0)" ::: "memory");
;         } else {
;             XB_SPIN(xb_ld(&bar[XB_XGEN(b.x)]) == gen, bar);
;             __builtin_amdgcn_fence(__ATOMIC_ACQUIRE, "agent");
;             asm volatile("s_waitcnt vmcnt(0)" ::: "memory");
.LBB0_928:
	s_or_b64 exec, exec, s[12:13]
	s_waitcnt vmcnt(0)
	buffer_inv sc1
	s_waitcnt vmcnt(0)
.LBB0_929:
	s_or_b64 exec, exec, s[6:7]
	s_waitcnt lgkmcnt(0)
	s_barrier

; __device__ __forceinline__ unsigned xb_ld(unsigned* p)              { return __hip_atomic_load(p, __ATOMIC_RELAXED, __HIP_MEMORY_SCOPE_AGENT); }
; __device__ __forceinline__ unsigned xb_add(unsigned* p, unsigned v) { return __hip_atomic_fetch_add(p, v, __ATOMIC_RELAXED, __HIP_MEMORY_SCOPE_AGENT); }
; #define XB_SPIN(cond, bar) do { unsigned _sp = 0; while (cond) { __builtin_amdgcn_s_sleep(1); \
;     if ((++_sp & 255u) == 0u) { if (xb_ld(&(bar)[XB_TMO])) break; if (_sp > XB_SPIN_CAP) { atomicAdd(&(bar)[XB_TMO], 1u); break; } } } } while (0)
; __device__ __forceinline__ void xcd_barrier(const XcdBarrier& b) {
;     ...
;             __builtin_amdgcn_fence(__ATOMIC_ACQUIRE, "agent");
;             xb_add(&bar[XB_XGEN(b.x)], 1u);
;             asm volatile("s_waitcnt vmcnt(0)" ::: "memory");
;         } else {
;             XB_SPIN(xb_ld(&bar[XB_XGEN(b.x)]) == gen, bar);
;             __builtin_amdgcn_fence(__ATOMIC_ACQUIRE, "agent");
;             asm volatile("s_waitcnt vmcnt(0)" ::: "memory");
.LBB0_1093:
	s_or_b64 exec, exec, s[12:13]
	s_waitcnt vmcnt(0)
	buffer_inv sc1
	s_waitcnt vmcnt(0)
.LBB0_1094:
	s_or_b64 exec, exec, s[6:7]
	s_waitcnt lgkmcnt(0)
	s_barrier

; __device__ __forceinline__ unsigned xb_ld(unsigned* p)              { return __hip_atomic_load(p, __ATOMIC_RELAXED, __HIP_MEMORY_SCOPE_AGENT); }
; __device__ __forceinline__ unsigned xb_add(unsigned* p, unsigned v) { return __hip_atomic_fetch_add(p, v, __ATOMIC_RELAXED, __HIP_MEMORY_SCOPE_AGENT); }
; #define XB_SPIN(cond, bar) do { unsigned _sp = 0; while (cond) { __builtin_amdgcn_s_sleep(1); \
;     if ((++_sp & 255u) == 0u) { if (xb_ld(&(bar)[XB_TMO])) break; if (_sp > XB_SPIN_CAP) { atomicAdd(&(bar)[XB_TMO], 1u); break; } } } } while (0)
; __device__ __forceinline__ void xcd_barrier(const XcdBarrier& b) {
;     ...
;             __builtin_amdgcn_fence(__ATOMIC_ACQUIRE, "agent");
;             xb_add(&bar[XB_XGEN(b.x)], 1u);
;             asm volatile("s_waitcnt vmcnt(0)" ::: "memory");
;         } else {
;             XB_SPIN(xb_ld(&bar[XB_XGEN(b.x)]) == gen, bar);
;             __builtin_amdgcn_fence(__ATOMIC_ACQUIRE, "agent");
;             asm volatile("s_waitcnt vmcnt(0)" ::: "memory");
.LBB0_1204:
	s_or_b64 exec, exec, s[12:13]
	s_waitcnt vmcnt(0)
	buffer_inv sc1
	s_waitcnt vmcnt(0)
.LBB0_1205:
	s_or_b64 exec, exec, s[6:7]
	s_waitcnt lgkmcnt(0)
	s_barrier

; __device__ __forceinline__ unsigned xb_ld(unsigned* p)              { return __hip_atomic_load(p, __ATOMIC_RELAXED, __HIP_MEMORY_SCOPE_AGENT); }
; __device__ __forceinline__ unsigned xb_add(unsigned* p, unsigned v) { return __hip_atomic_fetch_add(p, v, __ATOMIC_RELAXED, __HIP_MEMORY_SCOPE_AGENT); }
; #define XB_SPIN(cond, bar) do { unsigned _sp = 0; while (cond) { __builtin_amdgcn_s_sleep(1); \
;     if ((++_sp & 255u) == 0u) { if (xb_ld(&(bar)[XB_TMO])) break; if (_sp > XB_SPIN_CAP) { atomicAdd(&(bar)[XB_TMO], 1u); break; } } } } while (0)
; __device__ __forceinline__ void xcd_barrier(const XcdBarrier& b) {
;     ...
;             __builtin_amdgcn_fence(__ATOMIC_ACQUIRE, "agent");
;             xb_add(&bar[XB_XGEN(b.x)], 1u);
;             asm volatile("s_waitcnt vmcnt(0)" ::: "memory");
;         } else {
;             XB_SPIN(xb_ld(&bar[XB_XGEN(b.x)]) == gen, bar);
;             __builtin_amdgcn_fence(__ATOMIC_ACQUIRE, "agent");
;             asm volatile("s_waitcnt vmcnt(0)" ::: "memory");
.LBB0_1285:
	s_or_b64 exec, exec, s[12:13]
	s_waitcnt vmcnt(0)
	buffer_inv sc1
	s_waitcnt vmcnt(0)
.LBB0_1286:
	s_or_b64 exec, exec, s[6:7]
	s_waitcnt lgkmcnt(0)
	s_barrier

; __device__ __forceinline__ unsigned xb_ld(unsigned* p)              { return __hip_atomic_load(p, __ATOMIC_RELAXED, __HIP_MEMORY_SCOPE_AGENT); }
; __device__ __forceinline__ unsigned xb_add(unsigned* p, unsigned v) { return __hip_atomic_fetch_add(p, v, __ATOMIC_RELAXED, __HIP_MEMORY_SCOPE_AGENT); }
; #define XB_SPIN(cond, bar) do { unsigned _sp = 0; while (cond) { __builtin_amdgcn_s_sleep(1); \
;     if ((++_sp & 255u) == 0u) { if (xb_ld(&(bar)[XB_TMO])) break; if (_sp > XB_SPIN_CAP) { atomicAdd(&(bar)[XB_TMO], 1u); break; } } } } while (0)
; __device__ __forceinline__ void xcd_barrier(const XcdBarrier& b) {
;     ...
;             __builtin_amdgcn_fence(__ATOMIC_ACQUIRE, "agent");
;             xb_add(&bar[XB_XGEN(b.x)], 1u);
;             asm volatile("s_waitcnt vmcnt(0)" ::: "memory");
;         } else {
;             XB_SPIN(xb_ld(&bar[XB_XGEN(b.x)]) == gen, bar);
;             __builtin_amdgcn_fence(__ATOMIC_ACQUIRE, "agent");
;             asm volatile("s_waitcnt vmcnt(0)" ::: "memory");
.LBB0_1364:
	s_or_b64 exec, exec, s[12:13]
	s_waitcnt vmcnt(0)
	buffer_inv sc1
	s_waitcnt vmcnt(0)
.LBB0_1365:
	s_or_b64 exec, exec, s[6:7]
	s_waitcnt lgkmcnt(0)
	s_barrier

; __device__ __forceinline__ unsigned xb_ld(unsigned* p)              { return __hip_atomic_load(p, __ATOMIC_RELAXED, __HIP_MEMORY_SCOPE_AGENT); }
; __device__ __forceinline__ unsigned xb_add(unsigned* p, unsigned v) { return __hip_atomic_fetch_add(p, v, __ATOMIC_RELAXED, __HIP_MEMORY_SCOPE_AGENT); }
; #define XB_SPIN(cond, bar) do { unsigned _sp = 0; while (cond) { __builtin_amdgcn_s_sleep(1); \
;     if ((++_sp & 255u) == 0u) { if (xb_ld(&(bar)[XB_TMO])) break; if (_sp > XB_SPIN_CAP) { atomicAdd(&(bar)[XB_TMO], 1u); break; } } } } while (0)
; __device__ __forceinline__ void xcd_barrier(const XcdBarrier& b) {
;     ...
;             __builtin_amdgcn_fence(__ATOMIC_ACQUIRE, "agent");
;             xb_add(&bar[XB_XGEN(b.x)], 1u);
;             asm volatile("s_waitcnt vmcnt(0)" ::: "memory");
;         } else {
;             XB_SPIN(xb_ld(&bar[XB_XGEN(b.x)]) == gen, bar);
;             __builtin_amdgcn_fence(__ATOMIC_ACQUIRE, "agent");
;             asm volatile("s_waitcnt vmcnt(0)" ::: "memory");
.LBB0_1436:
	s_or_b64 exec, exec, s[12:13]
	s_waitcnt vmcnt(0)
	buffer_inv sc1
	s_waitcnt vmcnt(0)
.LBB0_1437:
	s_or_b64 exec, exec, s[6:7]
	s_waitcnt lgkmcnt(0)
	s_barrier

; __device__ __forceinline__ unsigned xb_ld(unsigned* p)              { return __hip_atomic_load(p, __ATOMIC_RELAXED, __HIP_MEMORY_SCOPE_AGENT); }
; __device__ __forceinline__ unsigned xb_add(unsigned* p, unsigned v) { return __hip_atomic_fetch_add(p, v, __ATOMIC_RELAXED, __HIP_MEMORY_SCOPE_AGENT); }
; #define XB_SPIN(cond, bar) do { unsigned _sp = 0; while (cond) { __builtin_amdgcn_s_sleep(1); \
;     if ((++_sp & 255u) == 0u) { if (xb_ld(&(bar)[XB_TMO])) break; if (_sp > XB_SPIN_CAP) { atomicAdd(&(bar)[XB_TMO], 1u); break; } } } } while (0)
; __device__ __forceinline__ void xcd_barrier(const XcdBarrier& b) {
;     ...
;             __builtin_amdgcn_fence(__ATOMIC_ACQUIRE, "agent");
;             xb_add(&bar[XB_XGEN(b.x)], 1u);
;             asm volatile("s_waitcnt vmcnt(0)" ::: "memory");
;         } else {
;             XB_SPIN(xb_ld(&bar[XB_XGEN(b.x)]) == gen, bar);
;             __builtin_amdgcn_fence(__ATOMIC_ACQUIRE, "agent");
;             asm volatile("s_waitcnt vmcnt(0)" ::: "memory");
.LBB0_1592:
	s_or_b64 exec, exec, s[12:13]
	s_waitcnt vmcnt(0)
	buffer_inv sc1
	s_waitcnt vmcnt(0)
.LBB0_1593:
	s_or_b64 exec, exec, s[6:7]
	s_waitcnt lgkmcnt(0)
	s_barrier

; __device__ __forceinline__ unsigned xb_ld(unsigned* p)              { return __hip_atomic_load(p, __ATOMIC_RELAXED, __HIP_MEMORY_SCOPE_AGENT); }
; __device__ __forceinline__ unsigned xb_add(unsigned* p, unsigned v) { return __hip_atomic_fetch_add(p, v, __ATOMIC_RELAXED, __HIP_MEMORY_SCOPE_AGENT); }
; #define XB_SPIN(cond, bar) do { unsigned _sp = 0; while (cond) { __builtin_amdgcn_s_sleep(1); \
;     if ((++_sp & 255u) == 0u) { if (xb_ld(&(bar)[XB_TMO])) break; if (_sp > XB_SPIN_CAP) { atomicAdd(&(bar)[XB_TMO], 1u); break; } } } } while (0)
; __device__ __forceinline__ void xcd_barrier(const XcdBarrier& b) {
;     ...
;             __builtin_amdgcn_fence(__ATOMIC_ACQUIRE, "agent");
;             xb_add(&bar[XB_XGEN(b.x)], 1u);
;             asm volatile("s_waitcnt vmcnt(0)" ::: "memory");
;         } else {
;             XB_SPIN(xb_ld(&bar[XB_XGEN(b.x)]) == gen, bar);
;             __builtin_amdgcn_fence(__ATOMIC_ACQUIRE, "agent");
;             asm volatile("s_waitcnt vmcnt(0)" ::: "memory");
.LBB0_1667:
	s_or_b64 exec, exec, s[12:13]
	s_waitcnt vmcnt(0)
	buffer_inv sc1
	s_waitcnt vmcnt(0)
.LBB0_1668:
	s_or_b64 exec, exec, s[6:7]
	s_waitcnt lgkmcnt(0)
	s_barrier

; __device__ __forceinline__ unsigned xb_ld(unsigned* p)              { return __hip_atomic_load(p, __ATOMIC_RELAXED, __HIP_MEMORY_SCOPE_AGENT); }
; __device__ __forceinline__ unsigned xb_add(unsigned* p, unsigned v) { return __hip_atomic_fetch_add(p, v, __ATOMIC_RELAXED, __HIP_MEMORY_SCOPE_AGENT); }
; #define XB_SPIN(cond, bar) do { unsigned _sp = 0; while (cond) { __builtin_amdgcn_s_sleep(1); \
;     if ((++_sp & 255u) == 0u) { if (xb_ld(&(bar)[XB_TMO])) break; if (_sp > XB_SPIN_CAP) { atomicAdd(&(bar)[XB_TMO], 1u); break; } } } } while (0)
; __device__ __forceinline__ void xcd_barrier(const XcdBarrier& b) {
;     ...
;             __builtin_amdgcn_fence(__ATOMIC_ACQUIRE, "agent");
;             xb_add(&bar[XB_XGEN(b.x)], 1u);
;             asm volatile("s_waitcnt vmcnt(0)" ::: "memory");
;         } else {
;             XB_SPIN(xb_ld(&bar[XB_XGEN(b.x)]) == gen, bar);
;             __builtin_amdgcn_fence(__ATOMIC_ACQUIRE, "agent");
;             asm volatile("s_waitcnt vmcnt(0)" ::: "memory");
.LBB0_1767:
	s_or_b64 exec, exec, s[8:9]
	s_mov_b64 s[8:9], exec
	v_mbcnt_lo_u32_b32 v0, s8, 0
	v_mbcnt_hi_u32_b32 v0, s9, v0
	v_cmp_eq_u32_e32 vcc, 0, v0
	s_and_saveexec_b64 s[10:11], vcc
	s_cbranch_execz .LBB0_1769
	s_bcnt1_i32_b64 s8, s[8:9]
	v_mov_b32_e32 v0, 0x2000
	v_mov_b32_e32 v1, s8
	global_atomic_add v0, v1, s[6:7] offset:1024
.LBB0_1769:
	s_or_b64 exec, exec, s[10:11]
	s_waitcnt vmcnt(0)
	buffer_inv sc1
	s_waitcnt vmcnt(0)
.LBB0_1770:
	s_or_b64 exec, exec, s[4:5]
	s_waitcnt lgkmcnt(0)
	s_barrier

; __device__ __forceinline__ unsigned xb_ld(unsigned* p)              { return __hip_atomic_load(p, __ATOMIC_RELAXED, __HIP_MEMORY_SCOPE_AGENT); }
; __device__ __forceinline__ unsigned xb_add(unsigned* p, unsigned v) { return __hip_atomic_fetch_add(p, v, __ATOMIC_RELAXED, __HIP_MEMORY_SCOPE_AGENT); }
; #define XB_SPIN(cond, bar) do { unsigned _sp = 0; while (cond) { __builtin_amdgcn_s_sleep(1); \
;     if ((++_sp & 255u) == 0u) { if (xb_ld(&(bar)[XB_TMO])) break; if (_sp > XB_SPIN_CAP) { atomicAdd(&(bar)[XB_TMO], 1u); break; } } } } while (0)
; __device__ __forceinline__ void xcd_barrier(const XcdBarrier& b) {
;     ...
;             __builtin_amdgcn_fence(__ATOMIC_ACQUIRE, "agent");
;             xb_add(&bar[XB_XGEN(b.x)], 1u);
;             asm volatile("s_waitcnt vmcnt(0)" ::: "memory");
;         } else {
;             XB_SPIN(xb_ld(&bar[XB_XGEN(b.x)]) == gen, bar);
;             __builtin_amdgcn_fence(__ATOMIC_ACQUIRE, "agent");
;             asm volatile("s_waitcnt vmcnt(0)" ::: "memory");
.LBB0_1827:
	s_or_b64 exec, exec, s[4:5]
	s_mov_b64 s[4:5], exec
	v_mbcnt_lo_u32_b32 v0, s4, 0
	v_mbcnt_hi_u32_b32 v0, s5, v0
	v_cmp_eq_u32_e32 vcc, 0, v0
	s_and_saveexec_b64 s[6:7], vcc
	s_cbranch_execz .LBB0_1829
	s_bcnt1_i32_b64 s4, s[4:5]
	v_mov_b32_e32 v0, 0x2000
	v_mov_b32_e32 v1, s4
	global_atomic_add v0, v1, s[2:3] offset:1024
.LBB0_1829:
	s_or_b64 exec, exec, s[6:7]
	s_waitcnt vmcnt(0)
	buffer_inv sc1
	s_waitcnt vmcnt(0)
.LBB0_1830:
	s_or_b64 exec, exec, s[0:1]
	s_waitcnt lgkmcnt(0)
	s_barrier
